# baseline (speedup 1.0000x reference)
_Z8dog_mainPKfS0_S0_S0_S0_S0_S0_Pf:
	s_load_dwordx8 s[12:19], s[0:1], 0x0
	s_load_dwordx8 s[20:27], s[0:1], 0x20
	s_and_b32 s3, s2, 7
	s_lshl_b32 s3, s3, 5
	s_lshr_b32 s4, s2, 3
	s_add_i32 s4, s3, s4
	s_and_b32 s6, s4, 3
	s_lshr_b32 s7, s4, 2
	s_mov_b32 s5, 0
	s_lshl_b64 s[8:9], s[4:5], 18
	v_and_b32_e32 v1, 63, v0
	v_lshrrev_b32_e32 v2, 6, v0
	v_and_b32_e32 v3, 15, v0
	v_and_b32_e32 v7, 31, v0
	v_lshl_or_b32 v5, v2, 5, v7
	v_lshlrev_b32_e32 v5, 2, v5
	v_mov_b32_e32 v4, v5
	v_lshlrev_b32_e32 v6, 4, v1
	v_lshl_or_b32 v6, v2, 12, v6
	v_bfe_u32 v7, v0, 4, 2
	v_readfirstlane_b32 s28, v2
	s_waitcnt lgkmcnt(0)
	global_load_dword v32, v4, s[18:19]
	global_load_dword v33, v4, s[20:21]
	global_load_dword v34, v4, s[22:23]
	global_load_dword v35, v4, s[24:25]
	global_load_dword v36, v4, s[14:15]
	global_load_dword v37, v4, s[16:17]
	s_add_u32 s12, s12, s8
	s_addc_u32 s13, s13, s9
	global_load_dwordx4 v[128:131], v6, s[12:13] offset:0 nt
	global_load_dwordx4 v[132:135], v6, s[12:13] offset:1024 nt
	global_load_dwordx4 v[136:139], v6, s[12:13] offset:2048 nt
	global_load_dwordx4 v[140:143], v6, s[12:13] offset:3072 nt
	v_add_u32_e32 v6, 0x8000, v6
	global_load_dwordx4 v[144:147], v6, s[12:13] offset:0 nt
	global_load_dwordx4 v[148:151], v6, s[12:13] offset:1024 nt
	global_load_dwordx4 v[152:155], v6, s[12:13] offset:2048 nt
	global_load_dwordx4 v[156:159], v6, s[12:13] offset:3072 nt
	s_cmp_ge_u32 s28, 4
	s_cbranch_scc0 .Lstag_skip
	s_sleep 16
